# v049 + nt policy on the retention scan's 8-byte output stores (read once by the next phase from other XCDs)
# speedup vs baseline: 1.0056x; 1.0056x over previous
; #define LAS __attribute__((address_space(3)))
; __device__ __forceinline__ unsigned cvt_pk_bf16(float lo, float hi) { const f32x2 v = {lo, hi}; const bf16v2_t r = __builtin_convertvector(v, bf16v2_t); return __builtin_bit_cast(unsigned, r); }
; __device__ __forceinline__ void ph_rscan(const int vc, const Params& p, LAS unsigned char* lds) {
;     ...
;         for (int ks = 0; ks < 8; ++ks) {
;             S = __builtin_amdgcn_mfma_f32_32x32x16_bf16(kf[ks], vs[ks], S, 0, 0, 0);
;             if (ks < 4 && att_need(ks)) {
; #pragma unroll
;                 for (int nt = 0; nt < 2; ++nt) oa[nt] = __builtin_amdgcn_mfma_f32_16x16x32_bf16(bv[2 * ks + nt], af[ks], oa[nt], 0, 0, 0); }
;         }
;         __builtin_amdgcn_sched_barrier(0);
;         { const bf16_t* apn = ATT + (size_t)cn * 16384 + (size_t)w * 4 * 512 + l * 8;
; #pragma unroll
;           for (int ks = 0; ks < 4; ++ks) { const int kse = att_need(ks) ? ks : (dir ? 3 : 0);
;               af[ks] = *(const bf16x8*)(apn + kse * 512); }
;           const bf16_t* kp = KT + (((size_t)h * 132 + (tbn >> 7)) * 8 + w) * 8 * 512 + l * 8;
; #pragma unroll
;           for (int ks = 0; ks < 8; ++ks) kf[ks] = *(const bf16x8*)(kp + ks * 512); }
;         {
;             bf16_t* obase = si < 2 ? dump : Ob + (size_t)tokbase(si) * 2048;
;             const int t = 16 * w + (l & 15); const float qs = qd[t];
;             bf16_t* orow = obase + (size_t)t * 2048 + h * 512 + sl * 32 + 4 * (l >> 4);
; #pragma unroll
;             for (int nt = 0; nt < 2; ++nt) { const f32x4 o = oi[nt] * qs + oa[nt]; u32x2 wv; wv.x = cvt_pk_bf16(o[0], o[1]); wv.y = cvt_pk_bf16(o[2], o[3]); *(u32x2*)(orow + 16 * nt) = wv; }
;         }
; #pragma unroll
;         for (int g = 0; g < 4; ++g) { u32x2 wv; wv.x = cvt_pk_bf16(S[4 * g], S[4 * g + 1]); wv.y = cvt_pk_bf16(S[4 * g + 2], S[4 * g + 3]);
;             *(LAS u32x2*)(STl + ((cur ^ 1) * 32 + (l & 31)) * RS_ST + 32 * w + 8 * g + 4 * (l >> 5)) = wv; }
;         stage_v(vnext, cur ^ 1);
.LBB0_1784:
	s_waitcnt vmcnt(14) lgkmcnt(3)
	v_mfma_f32_32x32x16_bf16 v[2:17], v[34:37], v[126:129], v[2:17]
	s_waitcnt vmcnt(13) lgkmcnt(2)
	v_mfma_f32_32x32x16_bf16 v[2:17], v[30:33], v[122:125], v[2:17]
	s_waitcnt vmcnt(12) lgkmcnt(1)
	v_mfma_f32_32x32x16_bf16 v[2:17], v[26:29], v[114:117], v[2:17]
	s_waitcnt vmcnt(11) lgkmcnt(0)
	v_mfma_f32_32x32x16_bf16 v[2:17], v[18:21], v[110:113], v[2:17]
	s_ashr_i32 s43, s42, 31
	s_lshl_b64 s[8:9], s[42:43], 15
	v_lshl_add_u64 v[18:19], v[194:195], 0, s[8:9]
	v_lshl_add_u64 v[20:21], v[18:19], 0, s[2:3]
	s_ashr_i32 s2, s40, 7
	s_ashr_i32 s9, s2, 31
	s_add_u32 s8, s2, s50
	s_mov_b32 s27, s3
	s_mov_b32 s29, s3
	s_mov_b32 s31, s3
	s_addc_u32 s9, s9, 0
	v_lshl_add_u64 v[22:23], v[18:19], 0, s[26:27]
	global_load_dwordx4 v[94:97], v[20:21], off
	global_load_dwordx4 v[90:93], v[22:23], off
	v_lshl_add_u64 v[20:21], v[18:19], 0, s[28:29]
	v_lshl_add_u64 v[18:19], v[18:19], 0, s[30:31]
	s_lshl_b64 s[8:9], s[8:9], 16
	global_load_dwordx4 v[82:85], v[20:21], off
	global_load_dwordx4 v[78:81], v[18:19], off
	v_lshl_add_u64 v[18:19], v[196:197], 0, s[8:9]
	v_add_co_u32_e32 v30, vcc, s51, v18
	global_load_dwordx4 v[86:89], v[18:19], off
	global_load_dwordx4 v[74:77], v[18:19], off offset:1024
	global_load_dwordx4 v[38:41], v[18:19], off offset:2048
	global_load_dwordx4 v[34:37], v[18:19], off offset:3072
	v_addc_co_u32_e32 v31, vcc, 0, v19, vcc
	global_load_dwordx4 v[18:21], v[30:31], off
	global_load_dwordx4 v[26:29], v[30:31], off offset:1024
	global_load_dwordx4 v[22:25], v[30:31], off offset:2048
	s_nop 0
	global_load_dwordx4 v[30:33], v[30:31], off offset:3072
	s_lshl_b32 s2, s59, 7
	s_add_i32 s8, s2, s55
	s_ashr_i32 s9, s8, 31
	s_lshl_b64 s[8:9], s[8:9], 12
	s_add_u32 s2, s47, s8
	ds_read_b32 v110, v205
	s_addc_u32 s10, s48, s9
	s_and_b64 s[8:9], s[38:39], exec
	s_cselect_b32 s9, s19, s10
	s_cselect_b32 s8, s18, s2
	v_lshl_add_u64 v[112:113], s[8:9], 0, v[200:201]
	s_mov_b32 s35, s3
	v_lshl_add_u64 v[112:113], v[112:113], 0, s[34:35]
	s_mov_b32 s37, s3
	s_waitcnt lgkmcnt(0)
	v_pk_fma_f32 v[100:101], v[100:101], v[110:111], v[104:105] op_sel_hi:[1,0,1]
	v_pk_fma_f32 v[98:99], v[98:99], v[110:111], v[102:103] op_sel_hi:[1,0,1]
	v_lshl_add_u64 v[112:113], v[112:113], 0, s[36:37]
	v_pk_fma_f32 v[108:109], v[108:109], v[110:111], v[120:121] op_sel_hi:[1,0,1]
	v_pk_fma_f32 v[106:107], v[106:107], v[110:111], v[118:119] op_sel_hi:[1,0,1]
	v_cvt_pk_bf16_f32 v102, v98, v99
	v_cvt_pk_bf16_f32 v103, v100, v101
	v_cvt_pk_bf16_f32 v98, v2, v3
	v_cvt_pk_bf16_f32 v99, v4, v5
	v_cvt_pk_bf16_f32 v100, v6, v7
	v_cvt_pk_bf16_f32 v101, v8, v9
	v_lshl_add_u64 v[112:113], v[112:113], 0, v[186:187]
	v_cvt_pk_bf16_f32 v106, v106, v107
	v_cvt_pk_bf16_f32 v107, v108, v109
	ds_write2_b64 v206, v[98:99], v[100:101] offset1:2
	v_cvt_pk_bf16_f32 v98, v10, v11
	v_cvt_pk_bf16_f32 v99, v12, v13
	v_cvt_pk_bf16_f32 v100, v14, v15
	v_cvt_pk_bf16_f32 v101, v16, v17
	global_store_dwordx2 v[112:113], v[106:107], off nt
	ds_write2_b64 v206, v[98:99], v[100:101] offset0:4 offset1:6
	s_waitcnt vmcnt(21)
	ds_write_b128 v1, v[130:133] offset:33792
	ds_read_b128 v[98:101], v199
	global_store_dwordx2 v[112:113], v[102:103], off offset:32 nt
	ds_read_b128 v[102:105], v199 offset:16
	v_lshlrev_b32_e32 v106, 16, v130
	v_and_b32_e32 v107, 0xffff0000, v130
	s_waitcnt lgkmcnt(1)
	v_pk_mul_f32 v[98:99], v[98:99], v[106:107]
	v_lshlrev_b32_e32 v106, 16, v131
	v_and_b32_e32 v107, 0xffff0000, v131
	v_pk_mul_f32 v[100:101], v[100:101], v[106:107]
	v_cvt_pk_bf16_f32 v98, v98, v99
	v_cvt_pk_bf16_f32 v99, v100, v101
	v_lshlrev_b32_e32 v100, 16, v132
	v_and_b32_e32 v101, 0xffff0000, v132
	s_waitcnt lgkmcnt(0)
	v_pk_mul_f32 v[100:101], v[102:103], v[100:101]
	v_lshlrev_b32_e32 v102, 16, v133
	v_and_b32_e32 v103, 0xffff0000, v133
	v_pk_mul_f32 v[102:103], v[104:105], v[102:103]
	s_add_i32 s2, s58, 2
	s_add_i32 s49, s49, 2
	s_add_i32 s57, s57, -2
	v_cvt_pk_bf16_f32 v100, v100, v101
	v_cvt_pk_bf16_f32 v101, v102, v103
	s_cmp_gt_u32 s58, 63
	s_mov_b32 s58, s2
	ds_write_b128 v1, v[98:101] offset:51200
	s_cbranch_scc1 .LBB0_1807

; #define LAS __attribute__((address_space(3)))
; __device__ __forceinline__ unsigned cvt_pk_bf16(float lo, float hi) { const f32x2 v = {lo, hi}; const bf16v2_t r = __builtin_convertvector(v, bf16v2_t); return __builtin_bit_cast(unsigned, r); }
; __device__ __forceinline__ void ph_rscan(const int vc, const Params& p, LAS unsigned char* lds) {
;     ...
;         __syncthreads();
;         const int sn = si + 1 < NSTEP ? si + 1 : si; const int tbn = tokbase(sn); const int cn = sn < 2 ? (dir ? 63 : 0) : chunk_of(sn);
;         const u32x4 vnext = *(const u32x4*)(vrow + tbn);
;         { const bf16_t* qp = Q + (((size_t)(b * 4 + h) * 512 + cn * 8 + w) * 8) * 512 + l * 8;
;     ...
;         {
;             bf16_t* obase = si < 2 ? dump : Ob + (size_t)tokbase(si) * 2048;
;             const int t = 16 * w + (l & 15); const float qs = qd[t];
;             bf16_t* orow = obase + (size_t)t * 2048 + h * 512 + sl * 32 + 4 * (l >> 4);
; #pragma unroll
;             for (int nt = 0; nt < 2; ++nt) { const f32x4 o = oi[nt] * qs + oa[nt]; u32x2 wv; wv.x = cvt_pk_bf16(o[0], o[1]); wv.y = cvt_pk_bf16(o[2], o[3]); *(u32x2*)(orow + 16 * nt) = wv; }
;         }
; #pragma unroll
;         for (int g = 0; g < 4; ++g) { u32x2 wv; wv.x = cvt_pk_bf16(S[4 * g], S[4 * g + 1]); wv.y = cvt_pk_bf16(S[4 * g + 2], S[4 * g + 3]);
;             *(LAS u32x2*)(STl + ((cur ^ 1) * 32 + (l & 31)) * RS_ST + 32 * w + 8 * g + 4 * (l >> 5)) = wv; }
;         stage_v(vnext, cur ^ 1);
.LBB0_1799:
	ds_read_b32 v50, v205
	v_lshl_add_u64 v[52:53], s[40:41], 0, v[200:201]
	s_mov_b32 s35, s3
	v_lshl_add_u64 v[52:53], v[52:53], 0, s[34:35]
	s_mov_b32 s37, s3
	v_lshl_add_u64 v[52:53], v[52:53], 0, s[36:37]
	s_waitcnt lgkmcnt(0)
	v_pk_fma_f32 v[48:49], v[48:49], v[50:51], v[136:137] op_sel_hi:[1,0,1]
	v_pk_fma_f32 v[46:47], v[46:47], v[50:51], v[134:135] op_sel_hi:[1,0,1]
	v_lshl_add_u64 v[52:53], v[52:53], 0, v[186:187]
	v_cvt_pk_bf16_f32 v46, v46, v47
	v_cvt_pk_bf16_f32 v47, v48, v49
	v_pk_fma_f32 v[44:45], v[44:45], v[50:51], v[68:69] op_sel_hi:[1,0,1]
	v_pk_fma_f32 v[42:43], v[42:43], v[50:51], v[66:67] op_sel_hi:[1,0,1]
	global_store_dwordx2 v[52:53], v[46:47], off nt
	v_cvt_pk_bf16_f32 v46, v42, v43
	v_cvt_pk_bf16_f32 v47, v44, v45
	v_cvt_pk_bf16_f32 v42, v2, v3
	v_cvt_pk_bf16_f32 v43, v4, v5
	v_cvt_pk_bf16_f32 v44, v6, v7
	v_cvt_pk_bf16_f32 v45, v8, v9
	v_add_u32_e32 v48, 0x4000, v206
	ds_write2_b64 v48, v[42:43], v[44:45] offset0:64 offset1:66
	v_cvt_pk_bf16_f32 v42, v10, v11
	v_cvt_pk_bf16_f32 v43, v12, v13
	v_cvt_pk_bf16_f32 v44, v14, v15
	v_cvt_pk_bf16_f32 v45, v16, v17
	ds_write2_b64 v48, v[42:43], v[44:45] offset0:68 offset1:70
	s_waitcnt vmcnt(21)
	ds_write_b128 v1, v[130:133] offset:42496
	ds_read_b128 v[42:45], v199
	global_store_dwordx2 v[52:53], v[46:47], off offset:32 nt
	ds_read_b128 v[46:49], v199 offset:16
	v_lshlrev_b32_e32 v50, 16, v130
	v_and_b32_e32 v51, 0xffff0000, v130
	s_or_b32 s27, s58, 1
	s_waitcnt lgkmcnt(1)
	v_pk_mul_f32 v[42:43], v[42:43], v[50:51]
	v_lshlrev_b32_e32 v50, 16, v131
	v_and_b32_e32 v51, 0xffff0000, v131
	v_pk_mul_f32 v[44:45], v[44:45], v[50:51]
	s_cmpk_lt_u32 s27, 0x41
	v_cvt_pk_bf16_f32 v42, v42, v43
	v_cvt_pk_bf16_f32 v43, v44, v45
	v_lshlrev_b32_e32 v44, 16, v132
	v_and_b32_e32 v45, 0xffff0000, v132
	s_cselect_b64 s[40:41], -1, 0
	s_waitcnt lgkmcnt(0)
	v_pk_mul_f32 v[44:45], v[46:47], v[44:45]
	v_lshlrev_b32_e32 v46, 16, v133
	v_and_b32_e32 v47, 0xffff0000, v133
	s_cmp_lg_u64 s[40:41], 0
	v_pk_mul_f32 v[46:47], v[48:49], v[46:47]
	s_addc_u32 s27, s49, 0
	v_cvt_pk_bf16_f32 v44, v44, v45
	v_cvt_pk_bf16_f32 v45, v46, v47
	s_cmp_lg_u64 s[40:41], 0
	ds_write_b128 v1, v[42:45] offset:59904
	v_sub_co_u32_e64 v42, s[42:43], s27, 2
	s_subb_u32 s27, 0, 0
	s_add_i32 s27, s57, s27
	s_and_b64 s[40:41], s[0:1], exec
	v_readfirstlane_b32 s29, v42
	s_cselect_b32 s27, s29, s27
	s_lshl_b32 s29, s27, 7
	s_add_i32 s29, s29, s55
	s_and_b64 s[40:41], s[42:43], exec
	s_cselect_b32 s42, s46, s27
	s_cselect_b32 s40, s56, s29
	s_lshl_b32 s27, s42, 3
	s_ashr_i32 s41, s40, 31
	s_ashr_i32 s29, s27, 31
	s_add_u32 s44, s52, s27
	s_addc_u32 s45, s53, s29
	s_lshl_b64 s[44:45], s[44:45], 13
	v_lshl_add_u64 v[42:43], s[40:41], 1, v[188:189]
	v_lshl_add_u64 v[44:45], v[192:193], 0, s[44:45]
	s_waitcnt lgkmcnt(0)
	s_barrier
; #define LAS __attribute__((address_space(3)))
; __device__ __forceinline__ void ph_rscan(const int vc, const Params& p, LAS unsigned char* lds) {
;     ...
;         const u32x4 vnext = *(const u32x4*)(vrow + tbn);
;         { const bf16_t* qp = Q + (((size_t)(b * 4 + h) * 512 + cn * 8 + w) * 8) * 512 + l * 8;
; #pragma unroll
;           for (int ks = 0; ks < 8; ++ks) qn[ks] = *(const bf16x8*)(qp + ks * 512); }
;         f32x4 oi[2], oa[2];
; #pragma unroll
;         for (int nt = 0; nt < 2; ++nt) { oi[nt] = (f32x4){0.f, 0.f, 0.f, 0.f}; oa[nt] = (f32x4){0.f, 0.f, 0.f, 0.f}; }
;         {   bf16x8 bs[16];
; #pragma unroll
;             for (int ks = 0; ks < 8; ++ks)
; #pragma unroll
;                 for (int nt = 0; nt < 2; ++nt) bs[2 * ks + nt] = *(const LAS bf16x8*)(STl + (cur * 32 + 16 * nt + (l & 15)) * RS_ST + 32 * ks + 8 * (l >> 4));
;             __builtin_amdgcn_sched_barrier(0);
; #pragma unroll
;             for (int ks = 0; ks < 8; ++ks)
; #pragma unroll
;                 for (int nt = 0; nt < 2; ++nt) oi[nt] = __builtin_amdgcn_mfma_f32_16x16x32_bf16(bs[2 * ks + nt], qf[ks], oi[nt], 0, 0, 0);
;         }
;         __builtin_amdgcn_sched_barrier(0);
;         bf16x8 bv[8], vs[8];
; #pragma unroll
;         for (int ks = 0; ks < 4; ++ks)
; #pragma unroll
;             for (int nt = 0; nt < 2; ++nt) bv[2 * ks + nt] = *(const LAS bf16x8*)(VTl + (cur * 32 + 16 * nt + (l & 15)) * RS_VT + 32 * ks + 8 * (l >> 4));
; #pragma unroll
;         for (int ks = 0; ks < 8; ++ks) vs[ks] = *(const LAS bf16x8*)(VSl + (cur * 32 + (l & 31)) * RS_VT + 16 * ks + 8 * (l >> 5));
; #pragma unroll
;         for (int i = 0; i < 16; ++i) S[i] *= cd;
;         __builtin_amdgcn_sched_barrier(0);
; #pragma unroll
;         for (int ks = 0; ks < 8; ++ks) {
;             S = __builtin_amdgcn_mfma_f32_32x32x16_bf16(kf[ks], vs[ks], S, 0, 0, 0);
;             if (ks < 4 && att_need(ks)) {
; #pragma unroll
;                 for (int nt = 0; nt < 2; ++nt) oa[nt] = __builtin_amdgcn_mfma_f32_16x16x32_bf16(bv[2 * ks + nt], af[ks], oa[nt], 0, 0, 0); }
	global_load_dwordx4 v[130:133], v[42:43], off
	global_load_dwordx4 v[70:73], v[44:45], off
	global_load_dwordx4 v[66:69], v[44:45], off offset:1024
	global_load_dwordx4 v[62:65], v[44:45], off offset:2048
	v_add_co_u32_e32 v42, vcc, s51, v44
	s_nop 1
	v_addc_co_u32_e32 v43, vcc, 0, v45, vcc
	global_load_dwordx4 v[58:61], v[44:45], off offset:3072
	global_load_dwordx4 v[54:57], v[42:43], off
	global_load_dwordx4 v[50:53], v[42:43], off offset:1024
	global_load_dwordx4 v[46:49], v[42:43], off offset:2048
	s_nop 0
	global_load_dwordx4 v[42:45], v[42:43], off offset:3072
	ds_read_b128 v[134:137], v209
	ds_read_b128 v[138:141], v209 offset:64
	ds_read_b128 v[142:145], v209 offset:8448
	ds_read_b128 v[146:149], v209 offset:8512
	ds_read_b128 v[150:153], v209 offset:128
	ds_read_b128 v[154:157], v209 offset:192
	ds_read_b128 v[158:161], v209 offset:8576
	ds_read_b128 v[162:165], v209 offset:8640
	ds_read_b128 v[166:169], v209 offset:256
	ds_read_b128 v[170:173], v209 offset:320
	ds_read_b128 v[174:177], v209 offset:8704
	ds_read_b128 v[178:181], v209 offset:8768
	ds_read_b128 v[182:185], v209 offset:384
	ds_read_b128 v[212:215], v209 offset:448
	ds_read_b128 v[216:219], v209 offset:8832
	ds_read_b128 v[220:223], v209 offset:8896
	s_waitcnt vmcnt(30) lgkmcnt(14)
	v_mfma_f32_16x16x32_bf16 v[134:137], v[134:137], v[114:117], 0
	s_waitcnt lgkmcnt(13)
	v_mfma_f32_16x16x32_bf16 v[114:117], v[142:145], v[114:117], 0
	s_waitcnt vmcnt(29)
	v_mfma_f32_16x16x32_bf16 v[134:137], v[138:141], v[106:109], v[134:137]
	s_waitcnt lgkmcnt(12)
	v_mfma_f32_16x16x32_bf16 v[106:109], v[146:149], v[106:109], v[114:117]
	s_waitcnt vmcnt(28) lgkmcnt(11)
	v_mfma_f32_16x16x32_bf16 v[114:117], v[150:153], v[98:101], v[134:137]
	s_waitcnt lgkmcnt(9)
	v_mfma_f32_16x16x32_bf16 v[98:101], v[158:161], v[98:101], v[106:109]
	s_waitcnt vmcnt(27)
	v_mfma_f32_16x16x32_bf16 v[106:109], v[154:157], v[118:121], v[114:117]
	s_waitcnt lgkmcnt(8)
	v_mfma_f32_16x16x32_bf16 v[98:101], v[162:165], v[118:121], v[98:101]
	s_waitcnt vmcnt(26) lgkmcnt(7)
	v_mfma_f32_16x16x32_bf16 v[106:109], v[166:169], v[126:129], v[106:109]
	s_waitcnt lgkmcnt(5)
	v_mfma_f32_16x16x32_bf16 v[98:101], v[174:177], v[126:129], v[98:101]
	s_waitcnt vmcnt(25)
	v_mfma_f32_16x16x32_bf16 v[106:109], v[170:173], v[122:125], v[106:109]
	s_waitcnt lgkmcnt(4)
	v_mfma_f32_16x16x32_bf16 v[98:101], v[178:181], v[122:125], v[98:101]
	s_waitcnt vmcnt(24) lgkmcnt(3)
	v_mfma_f32_16x16x32_bf16 v[106:109], v[182:185], v[110:113], v[106:109]
	s_waitcnt lgkmcnt(1)
	v_mfma_f32_16x16x32_bf16 v[98:101], v[216:219], v[110:113], v[98:101]
	s_waitcnt vmcnt(23)
	v_mfma_f32_16x16x32_bf16 v[106:109], v[212:215], v[102:105], v[106:109]
	s_waitcnt lgkmcnt(0)
	v_mfma_f32_16x16x32_bf16 v[98:101], v[220:223], v[102:105], v[98:101]
	ds_read_b128 v[178:181], v210 offset:33792
	ds_read_b128 v[158:161], v210 offset:33856
	ds_read_b128 v[170:173], v210 offset:38144
	ds_read_b128 v[162:165], v210 offset:38208
	ds_read_b128 v[146:149], v210 offset:33920
	ds_read_b128 v[134:137], v210 offset:33984
	ds_read_b128 v[150:153], v210 offset:38272
	ds_read_b128 v[138:141], v210 offset:38336
	ds_read_b128 v[102:105], v204 offset:59904
	ds_read_b128 v[166:169], v204 offset:59936
	ds_read_b128 v[154:157], v204 offset:59968
	ds_read_b128 v[142:145], v204 offset:60000
	ds_read_b128 v[126:129], v204 offset:60032
	ds_read_b128 v[122:125], v204 offset:60064
	ds_read_b128 v[114:117], v204 offset:60096
	ds_read_b128 v[110:113], v204 offset:60128
	v_mov_b32_e32 v191, v190
	v_pk_mul_f32 v[16:17], v[190:191], v[16:17]
	v_pk_mul_f32 v[14:15], v[190:191], v[14:15]
	v_pk_mul_f32 v[12:13], v[190:191], v[12:13]
	v_pk_mul_f32 v[10:11], v[190:191], v[10:11]
	v_pk_mul_f32 v[8:9], v[190:191], v[8:9]
	v_pk_mul_f32 v[6:7], v[190:191], v[6:7]
	v_pk_mul_f32 v[4:5], v[190:191], v[4:5]
	v_pk_mul_f32 v[2:3], v[202:203], v[2:3]
	s_waitcnt vmcnt(18) lgkmcnt(7)
	s_nop 0
	v_mfma_f32_32x32x16_bf16 v[2:17], v[94:97], v[102:105], v[2:17]
	v_mov_b32_e32 v174, 0
	s_and_b64 vcc, exec, s[8:9]
	v_mov_b32_e32 v175, 0
	v_mov_b32_e32 v176, 0
	v_mov_b32_e32 v177, 0
	v_mov_b32_e32 v182, 0
	v_mov_b32_e32 v183, 0
	v_mov_b32_e32 v184, 0
	v_mov_b32_e32 v185, 0
	v_mov_b32_e32 v118, 0
	v_mov_b32_e32 v119, 0
	v_mov_b32_e32 v120, 0
	v_mov_b32_e32 v121, 0
	v_mov_b32_e32 v102, 0
	v_mov_b32_e32 v103, 0
	v_mov_b32_e32 v104, 0
	v_mov_b32_e32 v105, 0
	s_cbranch_vccnz .LBB0_1801
	v_mfma_f32_16x16x32_bf16 v[174:177], v[178:181], v[90:93], 0
	v_mfma_f32_16x16x32_bf16 v[182:185], v[170:173], v[90:93], 0
	s_nop 6
	v_mov_b32_e32 v118, v174
	v_mov_b32_e32 v119, v175
	v_mov_b32_e32 v120, v176
	v_mov_b32_e32 v121, v177
	v_mov_b32_e32 v102, v182
	v_mov_b32_e32 v103, v183
	v_mov_b32_e32 v104, v184
	v_mov_b32_e32 v105, v185
